# grid barrier spin loops poll without s_sleep (s_sleep 1 -> s_nop 0 at all 30 sites)
# speedup vs baseline: 1.0008x; 1.0008x over previous
.LBB0_59:
	global_load_dword v16, v17, s[76:77] offset:1024 sc1
	global_load_dword v1, v17, s[76:77] offset:1280 sc1
	global_load_dword v2, v17, s[76:77] offset:1536 sc1
	global_load_dword v3, v17, s[76:77] offset:1792 sc1
	global_load_dword v4, v17, s[76:77] offset:2048 sc1
	global_load_dword v5, v17, s[76:77] offset:2304 sc1
	global_load_dword v6, v17, s[76:77] offset:2560 sc1
	global_load_dword v7, v17, s[76:77] offset:2816 sc1
	global_load_dword v8, v17, s[76:77] offset:3072 sc1
	global_load_dword v9, v17, s[76:77] offset:3328 sc1
	global_load_dword v10, v17, s[76:77] offset:3584 sc1
	global_load_dword v11, v17, s[76:77] offset:3840 sc1
	global_load_dword v12, v17, s[6:7] sc1
	global_load_dword v13, v17, s[8:9] sc1
	global_load_dword v14, v17, s[10:11] sc1
	global_load_dword v15, v17, s[12:13] sc1
	s_mov_b64 s[14:15], -1
	s_mov_b64 s[16:17], -1
	s_waitcnt vmcnt(14)
	v_add_u32_e32 v18, v1, v16
	s_waitcnt vmcnt(13)
	v_add_u32_e32 v18, v18, v2
	s_waitcnt vmcnt(12)
	v_add_u32_e32 v18, v18, v3
	s_waitcnt vmcnt(11)
	v_add_u32_e32 v18, v18, v4
	s_waitcnt vmcnt(10)
	v_add_u32_e32 v18, v18, v5
	s_waitcnt vmcnt(9)
	v_add_u32_e32 v18, v18, v6
	s_waitcnt vmcnt(8)
	v_add_u32_e32 v18, v18, v7
	s_waitcnt vmcnt(7)
	v_add_u32_e32 v18, v18, v8
	s_waitcnt vmcnt(6)
	v_add_u32_e32 v18, v18, v9
	s_waitcnt vmcnt(5)
	v_add_u32_e32 v18, v18, v10
	s_waitcnt vmcnt(4)
	v_add_u32_e32 v18, v18, v11
	s_waitcnt vmcnt(3)
	v_add_u32_e32 v18, v18, v12
	s_waitcnt vmcnt(2)
	v_add_u32_e32 v18, v18, v13
	s_waitcnt vmcnt(1)
	v_add_u32_e32 v18, v18, v14
	s_waitcnt vmcnt(0)
	v_add_u32_e32 v18, v18, v15
	v_cmp_eq_u32_e32 vcc, s2, v18
	s_cbranch_vccnz .LBB0_58
	s_and_b32 s14, s3, 0xff
	s_cmp_eq_u32 s14, 0
	s_mov_b64 s[14:15], -1
	s_mov_b64 s[18:19], -1
	s_nop 0
	s_cbranch_scc1 .LBB0_63
	s_and_b64 vcc, exec, s[18:19]
	s_cbranch_vccz .LBB0_58

.LBB0_77:
	s_and_b32 s3, s2, 0xff
	s_mov_b64 s[18:19], -1
	s_cmp_lg_u32 s3, 0
	s_mov_b64 s[22:23], -1
	s_nop 0
	s_cbranch_scc0 .LBB0_80
	s_and_b64 vcc, exec, s[22:23]
	s_cbranch_vccz .LBB0_76

.LBB0_94:
	s_and_b32 s3, s2, 0xff
	s_cmp_lg_u32 s3, 0
	s_mov_b64 s[22:23], -1
	s_nop 0
	s_cbranch_scc0 .LBB0_97
	s_mov_b64 s[24:25], -1
	s_and_b64 vcc, exec, s[22:23]
	s_cbranch_vccz .LBB0_93

.LBB0_413:
	global_load_dword v16, v17, s[76:77] offset:1024 sc1
	global_load_dword v1, v17, s[76:77] offset:1280 sc1
	global_load_dword v2, v17, s[76:77] offset:1536 sc1
	global_load_dword v3, v17, s[76:77] offset:1792 sc1
	global_load_dword v4, v17, s[76:77] offset:2048 sc1
	global_load_dword v5, v17, s[76:77] offset:2304 sc1
	global_load_dword v6, v17, s[76:77] offset:2560 sc1
	global_load_dword v7, v17, s[76:77] offset:2816 sc1
	global_load_dword v8, v17, s[76:77] offset:3072 sc1
	global_load_dword v9, v17, s[76:77] offset:3328 sc1
	global_load_dword v10, v17, s[76:77] offset:3584 sc1
	global_load_dword v11, v17, s[76:77] offset:3840 sc1
	global_load_dword v12, v17, s[8:9] sc1
	global_load_dword v13, v17, s[10:11] sc1
	global_load_dword v14, v17, s[12:13] sc1
	global_load_dword v15, v17, s[14:15] sc1
	s_mov_b64 s[16:17], -1
	s_mov_b64 s[18:19], -1
	s_waitcnt vmcnt(14)
	v_add_u32_e32 v18, v1, v16
	s_waitcnt vmcnt(13)
	v_add_u32_e32 v18, v18, v2
	s_waitcnt vmcnt(12)
	v_add_u32_e32 v18, v18, v3
	s_waitcnt vmcnt(11)
	v_add_u32_e32 v18, v18, v4
	s_waitcnt vmcnt(10)
	v_add_u32_e32 v18, v18, v5
	s_waitcnt vmcnt(9)
	v_add_u32_e32 v18, v18, v6
	s_waitcnt vmcnt(8)
	v_add_u32_e32 v18, v18, v7
	s_waitcnt vmcnt(7)
	v_add_u32_e32 v18, v18, v8
	s_waitcnt vmcnt(6)
	v_add_u32_e32 v18, v18, v9
	s_waitcnt vmcnt(5)
	v_add_u32_e32 v18, v18, v10
	s_waitcnt vmcnt(4)
	v_add_u32_e32 v18, v18, v11
	s_waitcnt vmcnt(3)
	v_add_u32_e32 v18, v18, v12
	s_waitcnt vmcnt(2)
	v_add_u32_e32 v18, v18, v13
	s_waitcnt vmcnt(1)
	v_add_u32_e32 v18, v18, v14
	s_waitcnt vmcnt(0)
	v_add_u32_e32 v18, v18, v15
	v_cmp_eq_u32_e32 vcc, s2, v18
	s_cbranch_vccnz .LBB0_412
	s_and_b32 s16, s3, 0xff
	s_cmp_eq_u32 s16, 0
	s_mov_b64 s[16:17], -1
	s_mov_b64 s[20:21], -1
	s_nop 0
	s_cbranch_scc1 .LBB0_417
	s_and_b64 vcc, exec, s[20:21]
	s_cbranch_vccz .LBB0_412

.LBB0_1003:
	global_load_dword v16, v17, s[76:77] offset:1024 sc1
	global_load_dword v1, v17, s[76:77] offset:1280 sc1
	global_load_dword v2, v17, s[76:77] offset:1536 sc1
	global_load_dword v3, v17, s[76:77] offset:1792 sc1
	global_load_dword v4, v17, s[76:77] offset:2048 sc1
	global_load_dword v5, v17, s[76:77] offset:2304 sc1
	global_load_dword v6, v17, s[76:77] offset:2560 sc1
	global_load_dword v7, v17, s[76:77] offset:2816 sc1
	global_load_dword v8, v17, s[76:77] offset:3072 sc1
	global_load_dword v9, v17, s[76:77] offset:3328 sc1
	global_load_dword v10, v17, s[76:77] offset:3584 sc1
	global_load_dword v11, v17, s[76:77] offset:3840 sc1
	global_load_dword v12, v17, s[62:63] sc1
	global_load_dword v13, v17, s[64:65] sc1
	global_load_dword v14, v17, s[66:67] sc1
	global_load_dword v15, v17, s[86:87] sc1
	s_mov_b64 s[6:7], -1
	s_mov_b64 s[8:9], -1
	s_waitcnt vmcnt(14)
	v_add_u32_e32 v18, v1, v16
	s_waitcnt vmcnt(13)
	v_add_u32_e32 v18, v18, v2
	s_waitcnt vmcnt(12)
	v_add_u32_e32 v18, v18, v3
	s_waitcnt vmcnt(11)
	v_add_u32_e32 v18, v18, v4
	s_waitcnt vmcnt(10)
	v_add_u32_e32 v18, v18, v5
	s_waitcnt vmcnt(9)
	v_add_u32_e32 v18, v18, v6
	s_waitcnt vmcnt(8)
	v_add_u32_e32 v18, v18, v7
	s_waitcnt vmcnt(7)
	v_add_u32_e32 v18, v18, v8
	s_waitcnt vmcnt(6)
	v_add_u32_e32 v18, v18, v9
	s_waitcnt vmcnt(5)
	v_add_u32_e32 v18, v18, v10
	s_waitcnt vmcnt(4)
	v_add_u32_e32 v18, v18, v11
	s_waitcnt vmcnt(3)
	v_add_u32_e32 v18, v18, v12
	s_waitcnt vmcnt(2)
	v_add_u32_e32 v18, v18, v13
	s_waitcnt vmcnt(1)
	v_add_u32_e32 v18, v18, v14
	s_waitcnt vmcnt(0)
	v_add_u32_e32 v18, v18, v15
	v_cmp_eq_u32_e32 vcc, s12, v18
	s_cbranch_vccnz .LBB0_1002
	s_and_b32 s6, s2, 0xff
	s_cmp_eq_u32 s6, 0
	s_mov_b64 s[6:7], -1
	s_mov_b64 s[10:11], -1
	s_nop 0
	s_cbranch_scc1 .LBB0_1007
	s_and_b64 vcc, exec, s[10:11]
	s_cbranch_vccz .LBB0_1002

.LBB0_1021:
	s_and_b32 s14, s2, 0xff
	s_mov_b64 s[38:39], -1
	s_cmp_lg_u32 s14, 0
	s_mov_b64 s[52:53], -1
	s_nop 0
	s_cbranch_scc0 .LBB0_1024
	s_and_b64 vcc, exec, s[52:53]
	s_cbranch_vccz .LBB0_1020

.LBB0_1038:
	s_and_b32 s14, s2, 0xff
	s_cmp_lg_u32 s14, 0
	s_mov_b64 s[50:51], -1
	s_nop 0
	s_cbranch_scc0 .LBB0_1041
	s_mov_b64 s[52:53], -1
	s_and_b64 vcc, exec, s[50:51]
	s_cbranch_vccz .LBB0_1037

.LBB0_1099:
	global_load_dword v16, v17, s[76:77] offset:1024 sc1
	global_load_dword v1, v17, s[76:77] offset:1280 sc1
	global_load_dword v2, v17, s[76:77] offset:1536 sc1
	global_load_dword v3, v17, s[76:77] offset:1792 sc1
	global_load_dword v4, v17, s[76:77] offset:2048 sc1
	global_load_dword v5, v17, s[76:77] offset:2304 sc1
	global_load_dword v6, v17, s[76:77] offset:2560 sc1
	global_load_dword v7, v17, s[76:77] offset:2816 sc1
	global_load_dword v8, v17, s[76:77] offset:3072 sc1
	global_load_dword v9, v17, s[76:77] offset:3328 sc1
	global_load_dword v10, v17, s[76:77] offset:3584 sc1
	global_load_dword v11, v17, s[76:77] offset:3840 sc1
	global_load_dword v12, v17, s[62:63] sc1
	global_load_dword v13, v17, s[64:65] sc1
	global_load_dword v14, v17, s[66:67] sc1
	global_load_dword v15, v17, s[86:87] sc1
	s_mov_b64 s[2:3], -1
	s_mov_b64 s[4:5], -1
	s_waitcnt vmcnt(14)
	v_add_u32_e32 v18, v1, v16
	s_waitcnt vmcnt(13)
	v_add_u32_e32 v18, v18, v2
	s_waitcnt vmcnt(12)
	v_add_u32_e32 v18, v18, v3
	s_waitcnt vmcnt(11)
	v_add_u32_e32 v18, v18, v4
	s_waitcnt vmcnt(10)
	v_add_u32_e32 v18, v18, v5
	s_waitcnt vmcnt(9)
	v_add_u32_e32 v18, v18, v6
	s_waitcnt vmcnt(8)
	v_add_u32_e32 v18, v18, v7
	s_waitcnt vmcnt(7)
	v_add_u32_e32 v18, v18, v8
	s_waitcnt vmcnt(6)
	v_add_u32_e32 v18, v18, v9
	s_waitcnt vmcnt(5)
	v_add_u32_e32 v18, v18, v10
	s_waitcnt vmcnt(4)
	v_add_u32_e32 v18, v18, v11
	s_waitcnt vmcnt(3)
	v_add_u32_e32 v18, v18, v12
	s_waitcnt vmcnt(2)
	v_add_u32_e32 v18, v18, v13
	s_waitcnt vmcnt(1)
	v_add_u32_e32 v18, v18, v14
	s_waitcnt vmcnt(0)
	v_add_u32_e32 v18, v18, v15
	v_cmp_eq_u32_e32 vcc, s9, v18
	s_cbranch_vccnz .LBB0_1098
	s_and_b32 s2, s8, 0xff
	s_cmp_eq_u32 s2, 0
	s_mov_b64 s[2:3], -1
	s_mov_b64 s[6:7], -1
	s_nop 0
	s_cbranch_scc1 .LBB0_1103
	s_and_b64 vcc, exec, s[6:7]
	s_cbranch_vccz .LBB0_1098

.LBB0_1117:
	s_and_b32 s12, s16, 0xff
	s_mov_b64 s[10:11], -1
	s_cmp_lg_u32 s12, 0
	s_mov_b64 s[14:15], -1
	s_nop 0
	s_cbranch_scc0 .LBB0_1120
	s_and_b64 vcc, exec, s[14:15]
	s_cbranch_vccz .LBB0_1116

.LBB0_1134:
	s_and_b32 s10, s16, 0xff
	s_cmp_lg_u32 s10, 0
	s_mov_b64 s[12:13], -1
	s_nop 0
	s_cbranch_scc0 .LBB0_1137
	s_mov_b64 s[14:15], -1
	s_and_b64 vcc, exec, s[12:13]
	s_cbranch_vccz .LBB0_1133
